# dedicated conversion workgroups: blockIdx mod 7 (37) with nt conversion stores
# speedup vs baseline: 1.0017x; 1.0015x over previous
.LBB0_454:
	s_cmp_gt_i32 s56, 3
	s_cselect_b64 s[0:1], -1, 0
	s_cmp_lt_i32 s57, 4
	s_cselect_b64 s[2:3], -1, 0
	s_or_b64 s[0:1], s[0:1], s[2:3]
	s_and_b64 vcc, exec, s[0:1]
	s_mul_i32 s46, s87, 0xb6db6db7
	s_cbranch_vccnz .LBB0_616
	s_mov_b32 s1, s46
	s_mov_b32 s0, 0x24924924
	v_mov_b32_e32 v2, s1
	v_mov_b32_e32 v1, v0
	v_cmp_lt_u32_e32 vcc, s0, v2
	s_nop 0
	v_cmp_eq_u32_e64 s[0:1], 0, v1
	s_cbranch_vccnz .LBB0_472
	s_mul_i32 s2, s91, 0x4100
	s_add_i32 s2, s2, 0
	s_add_u32 s10, s92, 0xa000000
	s_waitcnt lgkmcnt(0)
	v_and_b32_e32 v3, 7, v1
	v_bfe_u32 v7, v1, 3, 3
	s_addc_u32 s11, s93, 0
	v_lshlrev_b32_e32 v2, 2, v7
	v_mul_u32_u24_e32 v4, 0x810, v3
	v_add3_u32 v8, s2, v2, v4
	v_lshl_add_u32 v4, v3, 6, s2
	s_waitcnt vmcnt(0)
	v_mul_u32_u24_e32 v13, 0x204, v7
	s_add_u32 s12, s92, 0x2000000
	v_mov_b32_e32 v5, 0
	s_addc_u32 s13, s93, 0
	s_add_i32 s15, 0, 0x27c00
	v_add_u32_e32 v13, v4, v13
	s_mov_b32 s3, 0
	v_lshlrev_b32_e32 v6, 2, v3
	v_lshlrev_b32_e32 v2, 4, v3
	v_mov_b32_e32 v3, v5
	v_or_b32_e32 v9, 8, v7
	v_or_b32_e32 v10, 16, v7
	v_or_b32_e32 v11, 24, v7
	s_movk_i32 s14, 0x3ff
	v_mov_b32_e32 v12, s15
	s_movk_i32 s16, 0xbff
	s_mov_b32 s17, 0x8000
	s_mov_b32 s18, 0x10000
	s_mov_b32 s19, 0x18000
	s_mov_b32 s20, 0x20000
	s_mov_b32 s21, 0x28000
	s_mov_b32 s22, 0x30000
	s_mov_b32 s23, 0x38000
	s_mov_b32 s24, 0x40000
	s_mov_b32 s25, 0x48000
	s_mov_b32 s26, 0x50000
	s_mov_b32 s27, 0x58000
	s_mov_b32 s28, 0x60000
	s_mov_b32 s29, 0x68000
	s_mov_b32 s30, 0x70000
	s_mov_b32 s31, 0x78000
	s_mov_b32 s33, 0xc3e00000
	v_add_u32_e32 v14, 0x1020, v13
	v_add_u32_e32 v15, 0x1028, v13
	v_add_u32_e32 v16, 0x1030, v13
	v_add_u32_e32 v17, 0x1038, v13
	v_add_u32_e32 v18, 0x1040, v13
	v_add_u32_e32 v19, 0x1048, v13
	v_add_u32_e32 v20, 0x1050, v13
	v_add_u32_e32 v21, 0x1058, v13
	v_add_u32_e32 v22, 0x2040, v13
	v_add_u32_e32 v23, 0x2048, v13
	v_add_u32_e32 v24, 0x2050, v13
	v_add_u32_e32 v25, 0x2058, v13
	v_add_u32_e32 v26, 0x2060, v13
	v_add_u32_e32 v27, 0x2068, v13
	v_add_u32_e32 v28, 0x2070, v13
	v_add_u32_e32 v29, 0x2078, v13
	v_add_u32_e32 v30, 0x3060, v13
	v_add_u32_e32 v31, 0x3068, v13
	v_add_u32_e32 v32, 0x3070, v13
	v_add_u32_e32 v33, 0x3078, v13
	v_add_u32_e32 v34, 0x3080, v13
	v_add_u32_e32 v35, 0x3088, v13
	v_add_u32_e32 v36, 0x3090, v13
	v_add_u32_e32 v37, 0x3098, v13
	s_mov_b32 s34, 0x80000
	s_mov_b32 s35, 0x90000
	s_mov_b32 s38, 0xa0000
	s_mov_b32 s39, 0xb0000
	s_mov_b32 s40, 0xc0000
	s_mov_b32 s41, 0xd0000
	s_mov_b32 s42, 0xe0000
	s_mov_b32 s43, 0xf0000
	v_add_u32_e32 v38, 0x400, v8
	v_mov_b32_e32 v39, 0x43e00000
	s_branch .LBB0_459

.LBB0_616:
	s_cmp_gt_i32 s56, 4
	s_cselect_b64 s[0:1], -1, 0
	s_cmp_lt_i32 s57, 5
	s_cselect_b64 s[2:3], -1, 0
	s_or_b64 s[0:1], s[0:1], s[2:3]
	s_and_b64 vcc, exec, s[0:1]
	s_cbranch_vccnz .LBB0_749
	s_nop 0
	v_mov_b32_e32 v6, v0
	s_mov_b32 s0, 0x24924924
	v_mov_b32_e32 v2, s46
	v_cmp_lt_u32_e32 vcc, s0, v2
	v_and_b32_e32 v1, 63, v6
	s_and_b64 vcc, exec, vcc
	v_cmp_eq_u32_e64 s[0:1], 0, v6
	s_mul_i32 s14, s91, 0x4100
	v_and_b32_e32 v171, 7, v6
	v_lshrrev_b32_e32 v1, 3, v1
	s_cbranch_vccnz .LBB0_634
	s_add_i32 s2, s14, 0
	s_add_u32 s10, s92, 0xa000000
	s_addc_u32 s11, s93, 0
	v_lshlrev_b32_e32 v2, 2, v1
	s_waitcnt lgkmcnt(0)
	v_mul_u32_u24_e32 v3, 0x810, v171
	v_lshl_add_u32 v4, v171, 6, s2
	s_waitcnt vmcnt(0)
	v_mul_u32_u24_e32 v13, 0x204, v1
	s_add_u32 s12, s92, 0x2000000
	v_add3_u32 v8, s2, v2, v3
	v_mov_b32_e32 v5, 0
	s_addc_u32 s13, s93, 0
	s_add_i32 s16, 0, 0x27c00
	v_add_u32_e32 v13, v4, v13
	s_mov_b32 s3, 0
	v_lshlrev_b32_e32 v7, 2, v171
	v_lshlrev_b32_e32 v2, 4, v171
	v_mov_b32_e32 v3, v5
	v_or_b32_e32 v9, 8, v1
	v_or_b32_e32 v10, 16, v1
	v_or_b32_e32 v11, 24, v1
	s_movk_i32 s15, 0x1ff
	v_mov_b32_e32 v12, s16
	s_movk_i32 s17, 0xbff
	s_mov_b32 s18, 0x8000
	s_mov_b32 s19, 0x10000
	s_mov_b32 s20, 0x18000
	s_mov_b32 s21, 0x20000
	s_mov_b32 s22, 0x28000
	s_mov_b32 s23, 0x30000
	s_mov_b32 s24, 0x38000
	s_mov_b32 s25, 0x40000
	s_mov_b32 s26, 0x48000
	s_mov_b32 s27, 0x50000
	s_mov_b32 s28, 0x58000
	s_mov_b32 s29, 0x60000
	s_mov_b32 s30, 0x68000
	s_mov_b32 s31, 0x70000
	s_mov_b32 s33, 0x78000
	s_mov_b32 s34, 0xc3e00000
	v_add_u32_e32 v14, 0x1020, v13
	v_add_u32_e32 v15, 0x1028, v13
	v_add_u32_e32 v16, 0x1030, v13
	v_add_u32_e32 v17, 0x1038, v13
	v_add_u32_e32 v18, 0x1040, v13
	v_add_u32_e32 v19, 0x1048, v13
	v_add_u32_e32 v20, 0x1050, v13
	v_add_u32_e32 v21, 0x1058, v13
	v_add_u32_e32 v22, 0x2040, v13
	v_add_u32_e32 v23, 0x2048, v13
	v_add_u32_e32 v24, 0x2050, v13
	v_add_u32_e32 v25, 0x2058, v13
	v_add_u32_e32 v26, 0x2060, v13
	v_add_u32_e32 v27, 0x2068, v13
	v_add_u32_e32 v28, 0x2070, v13
	v_add_u32_e32 v29, 0x2078, v13
	v_add_u32_e32 v30, 0x3060, v13
	v_add_u32_e32 v31, 0x3068, v13
	v_add_u32_e32 v32, 0x3070, v13
	v_add_u32_e32 v33, 0x3078, v13
	v_add_u32_e32 v34, 0x3080, v13
	v_add_u32_e32 v35, 0x3088, v13
	v_add_u32_e32 v36, 0x3090, v13
	v_add_u32_e32 v37, 0x3098, v13
	s_mov_b32 s35, 0x80000
	s_mov_b32 s38, 0x90000
	s_mov_b32 s39, 0xa0000
	s_mov_b32 s40, 0xb0000
	s_mov_b32 s41, 0xc0000
	s_mov_b32 s42, 0xd0000
	s_mov_b32 s43, 0xe0000
	s_mov_b32 s44, 0xf0000
	v_add_u32_e32 v38, 0x400, v8
	v_mov_b32_e32 v39, 0x43e00000
	s_branch .LBB0_621
